# v44 + gate/up GEMM: leading half runs 2 epilogue groups before its alignment barrier (overlaps the trailing half's last MFMA block)
# baseline (speedup 1.0000x reference)
; #define PG8_BAR __builtin_amdgcn_s_barrier()
; __device__ __forceinline__ float sigm(float x) { return __builtin_amdgcn_rcpf(1.0f + __builtin_amdgcn_exp2f(-1.4426950408889634f * x)); }
; __device__ __forceinline__ u32x4 pack8(const f32x4 a, const f32x4 b) { u32x4 w; w.x = cvt_pk_bf16(a[0], a[1]); w.y = cvt_pk_bf16(a[2], a[3]); w.z = cvt_pk_bf16(b[0], b[1]); w.w = cvt_pk_bf16(b[2], b[3]); return w; }
; template <class Epi, class Sched, bool ALIGN_EPI = false, bool SP2 = false>
; __device__ __forceinline__ void gemm_phase(PG8_LAS unsigned char* lds, const Gemm g, const Sched& S, const Epi& E) {
;     ...
;         if constexpr (ALIGN_EPI) { if (wr == 0) PG8_BAR; }
;     __device__ __forceinline__ void operator()(const f32x4 (&acc)[2][2][4][2], const Unit& u, int wr, int wc, int fr, int fq) const {
;         const int row0 = u.pm * BM + wr * 64 + fr, col0 = u.pn * HALF + wc * 32 + 8 * fq;
; #pragma unroll
;         for (int ai = 0; ai < 2; ++ai)
; #pragma unroll
;             for (int m = 0; m < 4; ++m) {
;                 bf16_t* rowp = O + (size_t)(row0 + ai * HALF + m * 16) * ldc + col0;
;                 f32x4 h[2];
; #pragma unroll
;                 for (int n = 0; n < 2; ++n) { const f32x4 gt = acc[ai][0][m][n], up = acc[ai][1][m][n];
; #pragma unroll
;                     for (int e = 0; e < 4; ++e) h[n][e] = gt[e] * sigm(gt[e]) * up[e]; }
;                 *(u32x4*)rowp = pack8(h[0], h[1]);
;             }
.Lpeel_exit_0:
.LBB0_156:
	v_pk_mul_f32 v[160:161], v[128:129], s[82:83] op_sel:[0,1] op_sel_hi:[1,1]
	v_pk_mul_f32 v[162:163], v[130:131], s[82:83] op_sel:[0,1] op_sel_hi:[1,1]
	v_pk_mul_f32 v[164:165], v[120:121], s[82:83] op_sel:[0,1] op_sel_hi:[1,1]
	v_pk_mul_f32 v[166:167], v[122:123], s[82:83] op_sel:[0,1] op_sel_hi:[1,1]
	v_exp_f32_e32 v160, v160
	v_exp_f32_e32 v161, v161
	v_exp_f32_e32 v162, v162
	v_exp_f32_e32 v163, v163
	v_exp_f32_e32 v164, v164
	v_exp_f32_e32 v165, v165
	v_exp_f32_e32 v166, v166
	v_exp_f32_e32 v167, v167
	v_pk_add_f32 v[160:161], v[160:161], 1.0 op_sel_hi:[1,0]
	v_pk_add_f32 v[162:163], v[162:163], 1.0 op_sel_hi:[1,0]
	v_pk_add_f32 v[164:165], v[164:165], 1.0 op_sel_hi:[1,0]
	v_pk_add_f32 v[166:167], v[166:167], 1.0 op_sel_hi:[1,0]
	v_rcp_f32_e32 v160, v160
	v_rcp_f32_e32 v161, v161
	v_rcp_f32_e32 v162, v162
	v_rcp_f32_e32 v163, v163
	v_rcp_f32_e32 v164, v164
	v_rcp_f32_e32 v165, v165
	v_rcp_f32_e32 v166, v166
	v_rcp_f32_e32 v167, v167
	v_pk_mul_f32 v[160:161], v[128:129], v[160:161]
	v_pk_mul_f32 v[162:163], v[130:131], v[162:163]
	v_pk_mul_f32 v[164:165], v[120:121], v[164:165]
	v_pk_mul_f32 v[166:167], v[122:123], v[166:167]
	v_pk_mul_f32 v[124:125], v[160:161], v[124:125]
	v_pk_mul_f32 v[126:127], v[162:163], v[126:127]
	v_pk_mul_f32 v[120:121], v[164:165], v[116:117]
	v_pk_mul_f32 v[128:129], v[166:167], v[118:119]
	v_lshl_or_b32 v152, s21, 7, v148
	v_lshl_add_u32 v150, s20, 8, v2
	v_ashrrev_i32_e32 v153, 31, v152
	v_mov_b64_e32 v[144:145], s[8:9]
	v_mad_i64_i32 v[154:155], s[20:21], v150, s82, v[144:145]
	s_andn2_b64 vcc, exec, s[2:3]
	v_lshlrev_b64 v[116:117], 1, v[152:153]
	v_lshl_add_u64 v[122:123], v[154:155], 0, v[116:117]
	v_cvt_pk_bf16_f32 v118, v124, v125
	v_cvt_pk_bf16_f32 v119, v126, v127
	v_cvt_pk_bf16_f32 v120, v120, v121
	v_cvt_pk_bf16_f32 v121, v128, v129
	flat_store_dwordx4 v[122:123], v[118:121] sc1
	s_nop 1
	v_pk_mul_f32 v[160:161], v[112:113], s[82:83] op_sel:[0,1] op_sel_hi:[1,1]
	v_pk_mul_f32 v[162:163], v[114:115], s[82:83] op_sel:[0,1] op_sel_hi:[1,1]
	v_pk_mul_f32 v[164:165], v[104:105], s[82:83] op_sel:[0,1] op_sel_hi:[1,1]
	v_pk_mul_f32 v[166:167], v[106:107], s[82:83] op_sel:[0,1] op_sel_hi:[1,1]
	v_exp_f32_e32 v160, v160
	v_exp_f32_e32 v161, v161
	v_exp_f32_e32 v162, v162
	v_exp_f32_e32 v163, v163
	v_exp_f32_e32 v164, v164
	v_exp_f32_e32 v165, v165
	v_exp_f32_e32 v166, v166
	v_exp_f32_e32 v167, v167
	v_pk_add_f32 v[160:161], v[160:161], 1.0 op_sel_hi:[1,0]
	v_pk_add_f32 v[162:163], v[162:163], 1.0 op_sel_hi:[1,0]
	v_pk_add_f32 v[164:165], v[164:165], 1.0 op_sel_hi:[1,0]
	v_pk_add_f32 v[166:167], v[166:167], 1.0 op_sel_hi:[1,0]
	v_rcp_f32_e32 v160, v160
	v_rcp_f32_e32 v161, v161
	v_rcp_f32_e32 v162, v162
	v_rcp_f32_e32 v163, v163
	v_rcp_f32_e32 v164, v164
	v_rcp_f32_e32 v165, v165
	v_rcp_f32_e32 v166, v166
	v_rcp_f32_e32 v167, v167
	v_pk_mul_f32 v[160:161], v[112:113], v[160:161]
	v_pk_mul_f32 v[162:163], v[114:115], v[162:163]
	v_pk_mul_f32 v[164:165], v[104:105], v[164:165]
	v_pk_mul_f32 v[166:167], v[106:107], v[166:167]
	v_pk_mul_f32 v[108:109], v[160:161], v[108:109]
	v_pk_mul_f32 v[110:111], v[162:163], v[110:111]
	v_pk_mul_f32 v[112:113], v[164:165], v[100:101]
	v_mul_f32_e32 v106, v166, v102
	v_mul_f32_e32 v103, v167, v103
	v_or_b32_e32 v118, 16, v150
	v_mad_i64_i32 v[118:119], s[20:21], v118, s82, v[144:145]
	v_lshl_add_u64 v[104:105], v[118:119], 0, v[116:117]
	v_cvt_pk_bf16_f32 v100, v108, v109
	v_cvt_pk_bf16_f32 v101, v110, v111
	v_cvt_pk_bf16_f32 v102, v112, v113
	v_cvt_pk_bf16_f32 v103, v106, v103
	flat_store_dwordx4 v[104:105], v[100:103] sc1
	s_nop 1
	s_cmp_lg_u64 s[10:11], 0
	s_cbranch_scc0 .Lepi_bar_skip_0
	s_barrier
.Lepi_bar_skip_0:
	v_pk_mul_f32 v[160:161], v[96:97], s[82:83] op_sel:[0,1] op_sel_hi:[1,1]
	v_pk_mul_f32 v[162:163], v[98:99], s[82:83] op_sel:[0,1] op_sel_hi:[1,1]
	v_pk_mul_f32 v[164:165], v[88:89], s[82:83] op_sel:[0,1] op_sel_hi:[1,1]
	v_pk_mul_f32 v[166:167], v[90:91], s[82:83] op_sel:[0,1] op_sel_hi:[1,1]
	v_exp_f32_e32 v160, v160
	v_exp_f32_e32 v161, v161
	v_exp_f32_e32 v162, v162
	v_exp_f32_e32 v163, v163
	v_exp_f32_e32 v164, v164
	v_exp_f32_e32 v165, v165
	v_exp_f32_e32 v166, v166
	v_exp_f32_e32 v167, v167
	v_pk_add_f32 v[160:161], v[160:161], 1.0 op_sel_hi:[1,0]
	v_pk_add_f32 v[162:163], v[162:163], 1.0 op_sel_hi:[1,0]
	v_pk_add_f32 v[164:165], v[164:165], 1.0 op_sel_hi:[1,0]
	v_pk_add_f32 v[166:167], v[166:167], 1.0 op_sel_hi:[1,0]
	v_rcp_f32_e32 v160, v160
	v_rcp_f32_e32 v161, v161
	v_rcp_f32_e32 v162, v162
	v_rcp_f32_e32 v163, v163
	v_rcp_f32_e32 v164, v164
	v_rcp_f32_e32 v165, v165
	v_rcp_f32_e32 v166, v166
	v_rcp_f32_e32 v167, v167
	v_pk_mul_f32 v[160:161], v[96:97], v[160:161]
	v_pk_mul_f32 v[162:163], v[98:99], v[162:163]
	v_pk_mul_f32 v[164:165], v[88:89], v[164:165]
	v_pk_mul_f32 v[166:167], v[90:91], v[166:167]
	v_pk_mul_f32 v[92:93], v[160:161], v[92:93]
	v_pk_mul_f32 v[94:95], v[162:163], v[94:95]
	v_pk_mul_f32 v[96:97], v[164:165], v[84:85]
	v_mul_f32_e32 v90, v166, v86
	v_mul_f32_e32 v87, v167, v87
	v_or_b32_e32 v100, 32, v150
	v_mad_i64_i32 v[100:101], s[20:21], v100, s82, v[144:145]
	v_lshl_add_u64 v[88:89], v[100:101], 0, v[116:117]
	v_cvt_pk_bf16_f32 v84, v92, v93
	v_cvt_pk_bf16_f32 v85, v94, v95
	v_cvt_pk_bf16_f32 v86, v96, v97
	v_cvt_pk_bf16_f32 v87, v90, v87
	flat_store_dwordx4 v[88:89], v[84:87] sc1
	s_nop 1
	v_pk_mul_f32 v[160:161], v[80:81], s[82:83] op_sel:[0,1] op_sel_hi:[1,1]
	v_pk_mul_f32 v[162:163], v[82:83], s[82:83] op_sel:[0,1] op_sel_hi:[1,1]
	v_pk_mul_f32 v[164:165], v[72:73], s[82:83] op_sel:[0,1] op_sel_hi:[1,1]
	v_pk_mul_f32 v[166:167], v[74:75], s[82:83] op_sel:[0,1] op_sel_hi:[1,1]
	v_exp_f32_e32 v160, v160
; __device__ __forceinline__ float sigm(float x) { return __builtin_amdgcn_rcpf(1.0f + __builtin_amdgcn_exp2f(-1.4426950408889634f * x)); }
; __device__ __forceinline__ u32x4 pack8(const f32x4 a, const f32x4 b) { u32x4 w; w.x = cvt_pk_bf16(a[0], a[1]); w.y = cvt_pk_bf16(a[2], a[3]); w.z = cvt_pk_bf16(b[0], b[1]); w.w = cvt_pk_bf16(b[2], b[3]); return w; }
;     __device__ __forceinline__ void operator()(const f32x4 (&acc)[2][2][4][2], const Unit& u, int wr, int wc, int fr, int fq) const {
;     ...
;         for (int ai = 0; ai < 2; ++ai)
; #pragma unroll
;             for (int m = 0; m < 4; ++m) {
;                 bf16_t* rowp = O + (size_t)(row0 + ai * HALF + m * 16) * ldc + col0;
;                 f32x4 h[2];
; #pragma unroll
;                 for (int n = 0; n < 2; ++n) { const f32x4 gt = acc[ai][0][m][n], up = acc[ai][1][m][n];
; #pragma unroll
;                     for (int e = 0; e < 4; ++e) h[n][e] = gt[e] * sigm(gt[e]) * up[e]; }
;                 *(u32x4*)rowp = pack8(h[0], h[1]);
;             }
	v_exp_f32_e32 v161, v161
	v_exp_f32_e32 v162, v162
	v_exp_f32_e32 v163, v163
	v_exp_f32_e32 v164, v164
	v_exp_f32_e32 v165, v165
	v_exp_f32_e32 v166, v166
	v_exp_f32_e32 v167, v167
	v_pk_add_f32 v[160:161], v[160:161], 1.0 op_sel_hi:[1,0]
	v_pk_add_f32 v[162:163], v[162:163], 1.0 op_sel_hi:[1,0]
	v_pk_add_f32 v[164:165], v[164:165], 1.0 op_sel_hi:[1,0]
	v_pk_add_f32 v[166:167], v[166:167], 1.0 op_sel_hi:[1,0]
	v_rcp_f32_e32 v160, v160
	v_rcp_f32_e32 v161, v161
	v_rcp_f32_e32 v162, v162
	v_rcp_f32_e32 v163, v163
	v_rcp_f32_e32 v164, v164
	v_rcp_f32_e32 v165, v165
	v_rcp_f32_e32 v166, v166
	v_rcp_f32_e32 v167, v167
	v_pk_mul_f32 v[160:161], v[80:81], v[160:161]
	v_pk_mul_f32 v[162:163], v[82:83], v[162:163]
	v_pk_mul_f32 v[164:165], v[72:73], v[164:165]
	v_pk_mul_f32 v[166:167], v[74:75], v[166:167]
	v_pk_mul_f32 v[76:77], v[160:161], v[76:77]
	v_pk_mul_f32 v[78:79], v[162:163], v[78:79]
	v_pk_mul_f32 v[80:81], v[164:165], v[68:69]
	v_mul_f32_e32 v74, v166, v70
	v_mul_f32_e32 v71, v167, v71
	v_or_b32_e32 v84, 48, v150
	v_mad_i64_i32 v[84:85], s[20:21], v84, s82, v[144:145]
	v_lshl_add_u64 v[72:73], v[84:85], 0, v[116:117]
	v_cvt_pk_bf16_f32 v68, v76, v77
	v_cvt_pk_bf16_f32 v69, v78, v79
	v_cvt_pk_bf16_f32 v70, v80, v81
	v_cvt_pk_bf16_f32 v71, v74, v71
	flat_store_dwordx4 v[72:73], v[68:71] sc1
	s_nop 1
	v_pk_mul_f32 v[160:161], v[64:65], s[82:83] op_sel:[0,1] op_sel_hi:[1,1]
	v_pk_mul_f32 v[162:163], v[66:67], s[82:83] op_sel:[0,1] op_sel_hi:[1,1]
	v_pk_mul_f32 v[164:165], v[56:57], s[82:83] op_sel:[0,1] op_sel_hi:[1,1]
	v_pk_mul_f32 v[166:167], v[58:59], s[82:83] op_sel:[0,1] op_sel_hi:[1,1]
	v_exp_f32_e32 v160, v160
	v_exp_f32_e32 v161, v161
	v_exp_f32_e32 v162, v162
	v_exp_f32_e32 v163, v163
	v_exp_f32_e32 v164, v164
	v_exp_f32_e32 v165, v165
	v_exp_f32_e32 v166, v166
	v_exp_f32_e32 v167, v167
	v_pk_add_f32 v[160:161], v[160:161], 1.0 op_sel_hi:[1,0]
	v_pk_add_f32 v[162:163], v[162:163], 1.0 op_sel_hi:[1,0]
	v_pk_add_f32 v[164:165], v[164:165], 1.0 op_sel_hi:[1,0]
	v_pk_add_f32 v[166:167], v[166:167], 1.0 op_sel_hi:[1,0]
	v_rcp_f32_e32 v160, v160
	v_rcp_f32_e32 v161, v161
	v_rcp_f32_e32 v162, v162
	v_rcp_f32_e32 v163, v163
	v_rcp_f32_e32 v164, v164
	v_rcp_f32_e32 v165, v165
	v_rcp_f32_e32 v166, v166
	v_rcp_f32_e32 v167, v167
	v_pk_mul_f32 v[160:161], v[64:65], v[160:161]
	v_pk_mul_f32 v[162:163], v[66:67], v[162:163]
	v_pk_mul_f32 v[164:165], v[56:57], v[164:165]
	v_pk_mul_f32 v[166:167], v[58:59], v[166:167]
	v_pk_mul_f32 v[60:61], v[160:161], v[60:61]
	v_pk_mul_f32 v[62:63], v[162:163], v[62:63]
	v_pk_mul_f32 v[64:65], v[164:165], v[52:53]
	v_mul_f32_e32 v58, v166, v54
	v_mul_f32_e32 v55, v167, v55
	v_add_u32_e32 v68, 0x80, v150
	v_mad_i64_i32 v[68:69], s[20:21], v68, s82, v[144:145]
	v_lshl_add_u64 v[56:57], v[68:69], 0, v[116:117]
	v_cvt_pk_bf16_f32 v52, v60, v61
	v_cvt_pk_bf16_f32 v53, v62, v63
	v_cvt_pk_bf16_f32 v54, v64, v65
	v_cvt_pk_bf16_f32 v55, v58, v55
	flat_store_dwordx4 v[56:57], v[52:55] sc1
	s_nop 1
	v_pk_mul_f32 v[160:161], v[48:49], s[82:83] op_sel:[0,1] op_sel_hi:[1,1]
	v_pk_mul_f32 v[162:163], v[50:51], s[82:83] op_sel:[0,1] op_sel_hi:[1,1]
	v_pk_mul_f32 v[164:165], v[40:41], s[82:83] op_sel:[0,1] op_sel_hi:[1,1]
	v_pk_mul_f32 v[166:167], v[42:43], s[82:83] op_sel:[0,1] op_sel_hi:[1,1]
	v_exp_f32_e32 v160, v160
	v_exp_f32_e32 v161, v161
	v_exp_f32_e32 v162, v162
	v_exp_f32_e32 v163, v163
	v_exp_f32_e32 v164, v164
	v_exp_f32_e32 v165, v165
	v_exp_f32_e32 v166, v166
	v_exp_f32_e32 v167, v167
	v_pk_add_f32 v[160:161], v[160:161], 1.0 op_sel_hi:[1,0]
	v_pk_add_f32 v[162:163], v[162:163], 1.0 op_sel_hi:[1,0]
	v_pk_add_f32 v[164:165], v[164:165], 1.0 op_sel_hi:[1,0]
	v_pk_add_f32 v[166:167], v[166:167], 1.0 op_sel_hi:[1,0]
	v_rcp_f32_e32 v160, v160
	v_rcp_f32_e32 v161, v161
	v_rcp_f32_e32 v162, v162
	v_rcp_f32_e32 v163, v163
	v_rcp_f32_e32 v164, v164
	v_rcp_f32_e32 v165, v165
	v_rcp_f32_e32 v166, v166
	v_rcp_f32_e32 v167, v167
	v_pk_mul_f32 v[160:161], v[48:49], v[160:161]
	v_pk_mul_f32 v[162:163], v[50:51], v[162:163]
; #define PG8_BAR __builtin_amdgcn_s_barrier()
; __device__ __forceinline__ float sigm(float x) { return __builtin_amdgcn_rcpf(1.0f + __builtin_amdgcn_exp2f(-1.4426950408889634f * x)); }
; __device__ __forceinline__ u32x4 pack8(const f32x4 a, const f32x4 b) { u32x4 w; w.x = cvt_pk_bf16(a[0], a[1]); w.y = cvt_pk_bf16(a[2], a[3]); w.z = cvt_pk_bf16(b[0], b[1]); w.w = cvt_pk_bf16(b[2], b[3]); return w; }
; template <class Epi, class Sched, bool ALIGN_EPI = false, bool SP2 = false>
; __device__ __forceinline__ void gemm_phase(PG8_LAS unsigned char* lds, const Gemm g, const Sched& S, const Epi& E) {
;     ...
;         if (!has_next) break;
; #pragma unroll
;         for (int a = 0; a < 2; ++a)
; #pragma unroll
;             for (int b = 0; b < 2; ++b)
; #pragma unroll
;                 for (int m = 0; m < 4; ++m)
; #pragma unroll
;                     for (int n = 0; n < 2; ++n) acc[a][b][m][n] = (f32x4){0.f, 0.f, 0.f, 0.f};
;         cur = nxt; cA = nA; cB = nB; ++ui;
;         if constexpr (ALIGN_EPI) { if (wr == 1) PG8_BAR; }
;     __device__ __forceinline__ void operator()(const f32x4 (&acc)[2][2][4][2], const Unit& u, int wr, int wc, int fr, int fq) const {
;     ...
;         for (int ai = 0; ai < 2; ++ai)
; #pragma unroll
;             for (int m = 0; m < 4; ++m) {
;                 bf16_t* rowp = O + (size_t)(row0 + ai * HALF + m * 16) * ldc + col0;
;                 f32x4 h[2];
; #pragma unroll
;                 for (int n = 0; n < 2; ++n) { const f32x4 gt = acc[ai][0][m][n], up = acc[ai][1][m][n];
; #pragma unroll
;                     for (int e = 0; e < 4; ++e) h[n][e] = gt[e] * sigm(gt[e]) * up[e]; }
;                 *(u32x4*)rowp = pack8(h[0], h[1]);
;             }
	v_pk_mul_f32 v[164:165], v[40:41], v[164:165]
	v_pk_mul_f32 v[166:167], v[42:43], v[166:167]
	v_pk_mul_f32 v[44:45], v[160:161], v[44:45]
	v_pk_mul_f32 v[46:47], v[162:163], v[46:47]
	v_pk_mul_f32 v[48:49], v[164:165], v[36:37]
	v_mul_f32_e32 v42, v166, v38
	v_mul_f32_e32 v39, v167, v39
	v_add_u32_e32 v52, 0x90, v150
	v_mad_i64_i32 v[52:53], s[20:21], v52, s82, v[144:145]
	v_lshl_add_u64 v[40:41], v[52:53], 0, v[116:117]
	v_cvt_pk_bf16_f32 v36, v44, v45
	v_cvt_pk_bf16_f32 v37, v46, v47
	v_cvt_pk_bf16_f32 v38, v48, v49
	v_cvt_pk_bf16_f32 v39, v42, v39
	flat_store_dwordx4 v[40:41], v[36:39] sc1
	s_nop 1
	v_pk_mul_f32 v[160:161], v[32:33], s[82:83] op_sel:[0,1] op_sel_hi:[1,1]
	v_pk_mul_f32 v[162:163], v[34:35], s[82:83] op_sel:[0,1] op_sel_hi:[1,1]
	v_pk_mul_f32 v[164:165], v[24:25], s[82:83] op_sel:[0,1] op_sel_hi:[1,1]
	v_pk_mul_f32 v[166:167], v[26:27], s[82:83] op_sel:[0,1] op_sel_hi:[1,1]
	v_exp_f32_e32 v160, v160
	v_exp_f32_e32 v161, v161
	v_exp_f32_e32 v162, v162
	v_exp_f32_e32 v163, v163
	v_exp_f32_e32 v164, v164
	v_exp_f32_e32 v165, v165
	v_exp_f32_e32 v166, v166
	v_exp_f32_e32 v167, v167
	v_pk_add_f32 v[160:161], v[160:161], 1.0 op_sel_hi:[1,0]
	v_pk_add_f32 v[162:163], v[162:163], 1.0 op_sel_hi:[1,0]
	v_pk_add_f32 v[164:165], v[164:165], 1.0 op_sel_hi:[1,0]
	v_pk_add_f32 v[166:167], v[166:167], 1.0 op_sel_hi:[1,0]
	v_rcp_f32_e32 v160, v160
	v_rcp_f32_e32 v161, v161
	v_rcp_f32_e32 v162, v162
	v_rcp_f32_e32 v163, v163
	v_rcp_f32_e32 v164, v164
	v_rcp_f32_e32 v165, v165
	v_rcp_f32_e32 v166, v166
	v_rcp_f32_e32 v167, v167
	v_pk_mul_f32 v[160:161], v[32:33], v[160:161]
	v_pk_mul_f32 v[162:163], v[34:35], v[162:163]
	v_pk_mul_f32 v[164:165], v[24:25], v[164:165]
	v_pk_mul_f32 v[166:167], v[26:27], v[166:167]
	v_pk_mul_f32 v[28:29], v[160:161], v[28:29]
	v_pk_mul_f32 v[30:31], v[162:163], v[30:31]
	v_pk_mul_f32 v[32:33], v[164:165], v[20:21]
	v_mul_f32_e32 v26, v166, v22
	v_mul_f32_e32 v23, v167, v23
	v_add_u32_e32 v36, 0xa0, v150
	v_mad_i64_i32 v[36:37], s[20:21], v36, s82, v[144:145]
	v_lshl_add_u64 v[24:25], v[36:37], 0, v[116:117]
	v_cvt_pk_bf16_f32 v20, v28, v29
	v_cvt_pk_bf16_f32 v21, v30, v31
	v_cvt_pk_bf16_f32 v22, v32, v33
	v_cvt_pk_bf16_f32 v23, v26, v23
	flat_store_dwordx4 v[24:25], v[20:23] sc1
	s_nop 1
	v_pk_mul_f32 v[160:161], v[16:17], s[82:83] op_sel:[0,1] op_sel_hi:[1,1]
	v_pk_mul_f32 v[162:163], v[18:19], s[82:83] op_sel:[0,1] op_sel_hi:[1,1]
	v_pk_mul_f32 v[164:165], v[8:9], s[82:83] op_sel:[0,1] op_sel_hi:[1,1]
	v_pk_mul_f32 v[166:167], v[10:11], s[82:83] op_sel:[0,1] op_sel_hi:[1,1]
	v_exp_f32_e32 v160, v160
	v_exp_f32_e32 v161, v161
	v_exp_f32_e32 v162, v162
	v_exp_f32_e32 v163, v163
	v_exp_f32_e32 v164, v164
	v_exp_f32_e32 v165, v165
	v_exp_f32_e32 v166, v166
	v_exp_f32_e32 v167, v167
	v_pk_add_f32 v[160:161], v[160:161], 1.0 op_sel_hi:[1,0]
	v_pk_add_f32 v[162:163], v[162:163], 1.0 op_sel_hi:[1,0]
	v_pk_add_f32 v[164:165], v[164:165], 1.0 op_sel_hi:[1,0]
	v_pk_add_f32 v[166:167], v[166:167], 1.0 op_sel_hi:[1,0]
	v_rcp_f32_e32 v160, v160
	v_rcp_f32_e32 v161, v161
	v_rcp_f32_e32 v162, v162
	v_rcp_f32_e32 v163, v163
	v_rcp_f32_e32 v164, v164
	v_rcp_f32_e32 v165, v165
	v_rcp_f32_e32 v166, v166
	v_rcp_f32_e32 v167, v167
	v_pk_mul_f32 v[160:161], v[16:17], v[160:161]
	v_pk_mul_f32 v[162:163], v[18:19], v[162:163]
	v_pk_mul_f32 v[164:165], v[8:9], v[164:165]
	v_pk_mul_f32 v[166:167], v[10:11], v[166:167]
	v_pk_mul_f32 v[12:13], v[160:161], v[12:13]
	v_pk_mul_f32 v[14:15], v[162:163], v[14:15]
	v_pk_mul_f32 v[16:17], v[164:165], v[4:5]
	v_mul_f32_e32 v10, v166, v6
	v_mul_f32_e32 v7, v167, v7
	v_add_u32_e32 v20, 0xb0, v150
	v_mad_i64_i32 v[20:21], s[20:21], v20, s82, v[144:145]
	s_mov_b64 s[20:21], -1
	v_lshl_add_u64 v[8:9], v[20:21], 0, v[116:117]
	v_cvt_pk_bf16_f32 v4, v12, v13
	v_cvt_pk_bf16_f32 v5, v14, v15
	v_cvt_pk_bf16_f32 v6, v16, v17
	v_cvt_pk_bf16_f32 v7, v10, v7
	flat_store_dwordx4 v[8:9], v[4:7] sc1
	s_cbranch_vccnz .LBB0_149
	s_andn2_b64 vcc, exec, s[6:7]
	s_cbranch_vccnz .LBB0_148
	s_barrier
	s_branch .LBB0_148
